# v40 + fp8 GEMM K-loops: the two A-half LDS-DMA loads of each 6-load segment issued between the MFMAs of that segment's compute phase (wait becomes vmcnt(6))
# speedup vs baseline: 1.0030x; 1.0030x over previous
.LBB0_177:
	s_add_u32 s28, s4, s26
	s_addc_u32 s29, s5, s27
	s_add_u32 s30, s28, 0xe000100
	s_addc_u32 s31, s29, 0
	ds_read_b128 v[24:27], v252
	ds_read_b128 v[28:31], v253
	s_and_b64 s[28:29], s[34:35], exec
	ds_read_b128 v[16:19], v252 offset:2048
	ds_read_b128 v[20:23], v253 offset:2048
	s_cselect_b32 s29, s7, s31
	s_cselect_b32 s28, s6, s30
	s_add_u32 s61, s56, s26
	ds_read_b128 v[8:11], v252 offset:16384
	ds_read_b128 v[12:15], v253 offset:16384
	s_addc_u32 s62, s57, s27
	ds_read_b128 v[0:3], v252 offset:18432
	ds_read_b128 v[4:7], v253 offset:18432
	s_and_b64 s[30:31], s[34:35], exec
	s_cselect_b32 s31, s23, s62
	s_cselect_b32 s30, s22, s61
	s_add_u32 s61, s58, s26
	s_addc_u32 s62, s59, s27
	s_and_b64 s[34:35], s[34:35], exec
	s_cselect_b32 s35, s25, s62
	s_cselect_b32 s34, s24, s61
	s_add_u32 s100, s16, s26
	s_addc_u32 s101, s17, s27
	s_add_i32 m0, s37, 0xc000
	ds_read_b128 v[186:189], v206
	ds_read_b128 v[214:217], v206 offset:2048
	ds_read_b128 v[190:193], v207
	ds_read_b128 v[218:221], v207 offset:2048
	ds_read_b128 v[222:225], v206 offset:4096
	ds_read_b128 v[230:233], v206 offset:6144
	ds_read_b128 v[226:229], v207 offset:4096
	ds_read_b128 v[234:237], v207 offset:6144
	global_load_lds_dwordx4 v166, s[100:101]
	s_add_i32 m0, s37, 0xe000
	s_nop 0
	global_load_lds_dwordx4 v168, s[100:101]
	s_waitcnt vmcnt(8)
	s_waitcnt lgkmcnt(0)
	s_barrier
	s_setprio 1
	s_waitcnt lgkmcnt(0)
	v_mfma_f32_16x16x128_f8f6f4 v[156:159], v[24:31], v[186:193], v[156:159]
	v_mfma_f32_16x16x128_f8f6f4 v[152:155], v[16:23], v[186:193], v[152:155]
	v_mfma_f32_16x16x128_f8f6f4 v[144:147], v[24:31], v[214:221], v[144:147]
	v_mfma_f32_16x16x128_f8f6f4 v[136:139], v[16:23], v[214:221], v[136:139]
	v_mfma_f32_16x16x128_f8f6f4 v[128:131], v[24:31], v[222:229], v[128:131]
	v_mfma_f32_16x16x128_f8f6f4 v[120:123], v[16:23], v[222:229], v[120:123]
	v_mfma_f32_16x16x128_f8f6f4 v[112:115], v[24:31], v[230:237], v[112:115]
	v_mfma_f32_16x16x128_f8f6f4 v[104:107], v[16:23], v[230:237], v[104:107]
	v_mfma_f32_16x16x128_f8f6f4 v[148:151], v[8:15], v[186:193], v[148:151]
	v_mfma_f32_16x16x128_f8f6f4 v[140:143], v[0:7], v[186:193], v[140:143]
	v_mfma_f32_16x16x128_f8f6f4 v[132:135], v[8:15], v[214:221], v[132:135]
	v_mfma_f32_16x16x128_f8f6f4 v[124:127], v[0:7], v[214:221], v[124:127]
	v_mfma_f32_16x16x128_f8f6f4 v[116:119], v[8:15], v[222:229], v[116:119]
	v_mfma_f32_16x16x128_f8f6f4 v[108:111], v[0:7], v[222:229], v[108:111]
	v_mfma_f32_16x16x128_f8f6f4 v[100:103], v[8:15], v[230:237], v[100:103]
	v_mfma_f32_16x16x128_f8f6f4 v[96:99], v[0:7], v[230:237], v[96:99]
	s_setprio 0
	s_barrier
	s_add_i32 s61, s44, s36
	s_mov_b32 m0, s61
	ds_read_b128 v[214:217], v206 offset:16384
	ds_read_b128 v[222:225], v206 offset:18432
	ds_read_b128 v[218:221], v207 offset:16384
	ds_read_b128 v[226:229], v207 offset:18432
	ds_read_b128 v[230:233], v206 offset:20480
	ds_read_b128 v[238:241], v206 offset:22528
	ds_read_b128 v[234:237], v207 offset:20480
	ds_read_b128 v[242:245], v207 offset:22528
	global_load_lds_dwordx4 v160, s[30:31]
	s_add_i32 m0, s61, 0x2000
	s_add_i32 s98, s46, s36
	global_load_lds_dwordx4 v162, s[30:31]
	s_mov_b32 m0, s98
	s_nop 0
	global_load_lds_dwordx4 v160, s[34:35]
	s_add_i32 m0, s98, 0x2000
	v_mov_b32_e32 v173, v165
	global_load_lds_dwordx4 v162, s[34:35]
	s_waitcnt vmcnt(6)
	s_waitcnt lgkmcnt(0)
	s_barrier
	s_setprio 1
	s_waitcnt lgkmcnt(0)
	v_mfma_f32_16x16x128_f8f6f4 v[92:95], v[24:31], v[214:221], v[92:95]
	v_mfma_f32_16x16x128_f8f6f4 v[88:91], v[16:23], v[214:221], v[88:91]
	v_mfma_f32_16x16x128_f8f6f4 v[80:83], v[24:31], v[222:229], v[80:83]
	v_mfma_f32_16x16x128_f8f6f4 v[72:75], v[16:23], v[222:229], v[72:75]
	s_mov_b32 m0, s37
	v_mfma_f32_16x16x128_f8f6f4 v[64:67], v[24:31], v[230:237], v[64:67]
	global_load_lds_dwordx4 v164, s[28:29]
	v_mfma_f32_16x16x128_f8f6f4 v[56:59], v[16:23], v[230:237], v[56:59]
	v_mfma_f32_16x16x128_f8f6f4 v[48:51], v[24:31], v[238:245], v[48:51]
	v_mfma_f32_16x16x128_f8f6f4 v[40:43], v[16:23], v[238:245], v[40:43]
	v_mfma_f32_16x16x128_f8f6f4 v[84:87], v[8:15], v[214:221], v[84:87]
	s_mov_b32 m0, s38
	v_mfma_f32_16x16x128_f8f6f4 v[76:79], v[0:7], v[214:221], v[76:79]
	global_load_lds_dwordx4 v172, s[28:29]
	v_mfma_f32_16x16x128_f8f6f4 v[68:71], v[8:15], v[222:229], v[68:71]
	v_mfma_f32_16x16x128_f8f6f4 v[60:63], v[0:7], v[222:229], v[60:63]
	v_mfma_f32_16x16x128_f8f6f4 v[52:55], v[8:15], v[230:237], v[52:55]
	v_mfma_f32_16x16x128_f8f6f4 v[44:47], v[0:7], v[230:237], v[44:47]
	v_mfma_f32_16x16x128_f8f6f4 v[36:39], v[8:15], v[238:245], v[36:39]
	v_mfma_f32_16x16x128_f8f6f4 v[32:35], v[0:7], v[238:245], v[32:35]
	s_setprio 0
	s_barrier
	ds_read_b128 v[0:3], v252 offset:32768
	ds_read_b128 v[4:7], v253 offset:32768
	ds_read_b128 v[8:11], v252 offset:34816
	ds_read_b128 v[12:15], v253 offset:34816
	ds_read_b128 v[16:19], v252 offset:49152
	ds_read_b128 v[20:23], v253 offset:49152
	ds_read_b128 v[24:27], v252 offset:51200
	ds_read_b128 v[28:31], v253 offset:51200
	s_mov_b32 m0, s39
	ds_read_b128 v[214:217], v206 offset:32768
	ds_read_b128 v[222:225], v206 offset:34816
	ds_read_b128 v[218:221], v207 offset:32768
	ds_read_b128 v[226:229], v207 offset:34816
	ds_read_b128 v[230:233], v206 offset:36864
	ds_read_b128 v[238:241], v206 offset:38912
	ds_read_b128 v[234:237], v207 offset:36864
	ds_read_b128 v[242:245], v207 offset:38912
	global_load_lds_dwordx4 v184, s[28:29]
	s_mov_b32 m0, s40
	s_nop 0
	global_load_lds_dwordx4 v182, s[28:29]
	s_waitcnt vmcnt(8)
	s_waitcnt lgkmcnt(0)
	s_barrier
	s_setprio 1
	s_waitcnt lgkmcnt(0)
	v_mfma_f32_16x16x128_f8f6f4 v[156:159], v[0:7], v[214:221], v[156:159]
	v_mfma_f32_16x16x128_f8f6f4 v[152:155], v[8:15], v[214:221], v[152:155]
	v_mfma_f32_16x16x128_f8f6f4 v[144:147], v[0:7], v[222:229], v[144:147]
	v_mfma_f32_16x16x128_f8f6f4 v[136:139], v[8:15], v[222:229], v[136:139]
	v_mfma_f32_16x16x128_f8f6f4 v[128:131], v[0:7], v[230:237], v[128:131]
	v_mfma_f32_16x16x128_f8f6f4 v[120:123], v[8:15], v[230:237], v[120:123]
	v_mfma_f32_16x16x128_f8f6f4 v[112:115], v[0:7], v[238:245], v[112:115]
	v_mfma_f32_16x16x128_f8f6f4 v[104:107], v[8:15], v[238:245], v[104:107]
	v_mfma_f32_16x16x128_f8f6f4 v[148:151], v[16:23], v[214:221], v[148:151]
	v_mfma_f32_16x16x128_f8f6f4 v[140:143], v[24:31], v[214:221], v[140:143]
	v_mfma_f32_16x16x128_f8f6f4 v[132:135], v[16:23], v[222:229], v[132:135]
	v_mfma_f32_16x16x128_f8f6f4 v[124:127], v[24:31], v[222:229], v[124:127]
	v_mfma_f32_16x16x128_f8f6f4 v[116:119], v[16:23], v[230:237], v[116:119]
	v_mfma_f32_16x16x128_f8f6f4 v[108:111], v[24:31], v[230:237], v[108:111]
	v_mfma_f32_16x16x128_f8f6f4 v[100:103], v[16:23], v[238:245], v[100:103]
	v_mfma_f32_16x16x128_f8f6f4 v[96:99], v[24:31], v[238:245], v[96:99]
	s_setprio 0
	s_barrier
	s_add_i32 s99, s36, 0x17f80
	s_mov_b32 m0, s99
	ds_read_b128 v[214:217], v206 offset:49152
	ds_read_b128 v[222:225], v206 offset:51200
	ds_read_b128 v[218:221], v207 offset:49152
	ds_read_b128 v[226:229], v207 offset:51200
	ds_read_b128 v[230:233], v206 offset:53248
	ds_read_b128 v[238:241], v206 offset:55296
	ds_read_b128 v[234:237], v207 offset:53248
	ds_read_b128 v[242:245], v207 offset:55296
	global_load_lds_dwordx4 v160, s[30:31] offset:128
	s_add_i32 m0, s99, 0x2000
	s_add_i32 s99, s36, 0x1bf80
	global_load_lds_dwordx4 v162, s[30:31] offset:128
	s_mov_b32 m0, s99
	s_nop 0
	global_load_lds_dwordx4 v160, s[34:35] offset:128
	s_add_i32 m0, s99, 0x2000
	s_nop 0
	global_load_lds_dwordx4 v162, s[34:35] offset:128
	s_waitcnt vmcnt(6)
	s_waitcnt lgkmcnt(0)
	s_barrier
	s_setprio 1
	s_waitcnt lgkmcnt(0)
	v_mfma_f32_16x16x128_f8f6f4 v[92:95], v[0:7], v[214:221], v[92:95]
	v_mfma_f32_16x16x128_f8f6f4 v[88:91], v[8:15], v[214:221], v[88:91]
	v_mfma_f32_16x16x128_f8f6f4 v[80:83], v[0:7], v[222:229], v[80:83]
	v_mfma_f32_16x16x128_f8f6f4 v[72:75], v[8:15], v[222:229], v[72:75]
	s_add_i32 m0, s41, 0xffffff80
	v_mfma_f32_16x16x128_f8f6f4 v[64:67], v[0:7], v[230:237], v[64:67]
	global_load_lds_dwordx4 v164, s[28:29] offset:128
	v_mfma_f32_16x16x128_f8f6f4 v[56:59], v[8:15], v[230:237], v[56:59]
	v_mfma_f32_16x16x128_f8f6f4 v[48:51], v[0:7], v[238:245], v[48:51]
	v_mfma_f32_16x16x128_f8f6f4 v[40:43], v[8:15], v[238:245], v[40:43]
	v_mfma_f32_16x16x128_f8f6f4 v[84:87], v[16:23], v[214:221], v[84:87]
	s_add_i32 m0, s42, 0xffffff80
	v_mfma_f32_16x16x128_f8f6f4 v[76:79], v[24:31], v[214:221], v[76:79]
	global_load_lds_dwordx4 v172, s[28:29] offset:128
	v_mfma_f32_16x16x128_f8f6f4 v[68:71], v[16:23], v[222:229], v[68:71]
	v_mfma_f32_16x16x128_f8f6f4 v[60:63], v[24:31], v[222:229], v[60:63]
	v_mfma_f32_16x16x128_f8f6f4 v[52:55], v[16:23], v[230:237], v[52:55]
	v_mfma_f32_16x16x128_f8f6f4 v[44:47], v[24:31], v[230:237], v[44:47]
	v_mfma_f32_16x16x128_f8f6f4 v[36:39], v[16:23], v[238:245], v[36:39]
	v_mfma_f32_16x16x128_f8f6f4 v[32:35], v[24:31], v[238:245], v[32:35]
	s_setprio 0
	s_barrier
	s_add_i32 s60, s60, 2
	s_add_u32 s26, s26, 0x100
	s_addc_u32 s27, s27, 0
	s_cmp_gt_u32 s60, 5
	s_cbranch_scc1 .LBB0_180

.LBB0_590:
	s_add_u32 s36, s8, s4
	s_addc_u32 s37, s9, s5
	s_add_u32 s38, s36, 0xe000100
	s_addc_u32 s39, s37, 0
	ds_read_b128 v[24:27], v252
	ds_read_b128 v[28:31], v253
	s_and_b64 s[36:37], s[40:41], exec
	ds_read_b128 v[16:19], v252 offset:2048
	ds_read_b128 v[20:23], v253 offset:2048
	s_cselect_b32 s37, s11, s39
	s_cselect_b32 s36, s10, s38
	s_add_u32 s90, s27, s4
	ds_read_b128 v[8:11], v252 offset:16384
	ds_read_b128 v[12:15], v253 offset:16384
	s_addc_u32 s91, s86, s5
	ds_read_b128 v[0:3], v252 offset:18432
	ds_read_b128 v[4:7], v253 offset:18432
	s_and_b64 s[38:39], s[40:41], exec
	s_cselect_b32 s39, s29, s91
	s_cselect_b32 s38, s28, s90
	s_add_u32 s90, s87, s4
	s_addc_u32 s91, s88, s5
	s_and_b64 s[40:41], s[40:41], exec
	s_cselect_b32 s41, s31, s91
	s_cselect_b32 s40, s30, s90
	s_add_u32 s100, s18, s4
	s_addc_u32 s101, s19, s5
	s_add_i32 m0, s61, 0xc000
	ds_read_b128 v[182:185], v201
	ds_read_b128 v[210:213], v201 offset:2048
	ds_read_b128 v[186:189], v202
	ds_read_b128 v[214:217], v202 offset:2048
	ds_read_b128 v[218:221], v201 offset:4096
	ds_read_b128 v[226:229], v201 offset:6144
	ds_read_b128 v[222:225], v202 offset:4096
	ds_read_b128 v[230:233], v202 offset:6144
	global_load_lds_dwordx4 v170, s[100:101]
	s_add_i32 m0, s61, 0xe000
	s_nop 0
	global_load_lds_dwordx4 v168, s[100:101]
	s_waitcnt vmcnt(8)
	s_waitcnt lgkmcnt(0)
	s_barrier
	s_setprio 1
	s_waitcnt lgkmcnt(0)
	v_mfma_f32_16x16x128_f8f6f4 v[156:159], v[24:31], v[182:189], v[156:159]
	v_mfma_f32_16x16x128_f8f6f4 v[148:151], v[16:23], v[182:189], v[148:151]
	v_mfma_f32_16x16x128_f8f6f4 v[140:143], v[24:31], v[210:217], v[140:143]
	v_mfma_f32_16x16x128_f8f6f4 v[132:135], v[16:23], v[210:217], v[132:135]
	v_mfma_f32_16x16x128_f8f6f4 v[124:127], v[24:31], v[218:225], v[124:127]
	v_mfma_f32_16x16x128_f8f6f4 v[116:119], v[16:23], v[218:225], v[116:119]
	v_mfma_f32_16x16x128_f8f6f4 v[108:111], v[24:31], v[226:233], v[108:111]
	v_mfma_f32_16x16x128_f8f6f4 v[100:103], v[16:23], v[226:233], v[100:103]
	v_mfma_f32_16x16x128_f8f6f4 v[152:155], v[8:15], v[182:189], v[152:155]
	v_mfma_f32_16x16x128_f8f6f4 v[144:147], v[0:7], v[182:189], v[144:147]
	v_mfma_f32_16x16x128_f8f6f4 v[136:139], v[8:15], v[210:217], v[136:139]
	v_mfma_f32_16x16x128_f8f6f4 v[128:131], v[0:7], v[210:217], v[128:131]
	v_mfma_f32_16x16x128_f8f6f4 v[120:123], v[8:15], v[218:225], v[120:123]
	v_mfma_f32_16x16x128_f8f6f4 v[112:115], v[0:7], v[218:225], v[112:115]
	v_mfma_f32_16x16x128_f8f6f4 v[104:107], v[8:15], v[226:233], v[104:107]
	v_mfma_f32_16x16x128_f8f6f4 v[96:99], v[0:7], v[226:233], v[96:99]
	s_setprio 0
	s_barrier
	s_add_i32 s90, s72, s44
	s_mov_b32 m0, s90
	ds_read_b128 v[210:213], v201 offset:16384
	ds_read_b128 v[218:221], v201 offset:18432
	ds_read_b128 v[214:217], v202 offset:16384
	ds_read_b128 v[222:225], v202 offset:18432
	ds_read_b128 v[226:229], v201 offset:20480
	ds_read_b128 v[234:237], v201 offset:22528
	ds_read_b128 v[230:233], v202 offset:20480
	ds_read_b128 v[238:241], v202 offset:22528
	global_load_lds_dwordx4 v160, s[38:39]
	s_add_i32 m0, s90, 0x2000
	s_add_i32 s98, s74, s44
	global_load_lds_dwordx4 v162, s[38:39]
	s_mov_b32 m0, s98
	s_nop 0
	global_load_lds_dwordx4 v160, s[40:41]
	s_add_i32 m0, s98, 0x2000
	v_mov_b32_e32 v167, v165
	global_load_lds_dwordx4 v162, s[40:41]
	s_waitcnt vmcnt(6)
	s_waitcnt lgkmcnt(0)
	s_barrier
	s_setprio 1
	s_waitcnt lgkmcnt(0)
	v_mfma_f32_16x16x128_f8f6f4 v[92:95], v[24:31], v[210:217], v[92:95]
	v_mfma_f32_16x16x128_f8f6f4 v[84:87], v[16:23], v[210:217], v[84:87]
	v_mfma_f32_16x16x128_f8f6f4 v[76:79], v[24:31], v[218:225], v[76:79]
	v_mfma_f32_16x16x128_f8f6f4 v[68:71], v[16:23], v[218:225], v[68:71]
	s_mov_b32 m0, s61
	v_mfma_f32_16x16x128_f8f6f4 v[60:63], v[24:31], v[226:233], v[60:63]
	global_load_lds_dwordx4 v164, s[36:37]
	v_mfma_f32_16x16x128_f8f6f4 v[52:55], v[16:23], v[226:233], v[52:55]
	v_mfma_f32_16x16x128_f8f6f4 v[44:47], v[24:31], v[234:241], v[44:47]
	v_mfma_f32_16x16x128_f8f6f4 v[36:39], v[16:23], v[234:241], v[36:39]
	v_mfma_f32_16x16x128_f8f6f4 v[88:91], v[8:15], v[210:217], v[88:91]
	s_mov_b32 m0, s62
	v_mfma_f32_16x16x128_f8f6f4 v[80:83], v[0:7], v[210:217], v[80:83]
	global_load_lds_dwordx4 v166, s[36:37]
	v_mfma_f32_16x16x128_f8f6f4 v[72:75], v[8:15], v[218:225], v[72:75]
	v_mfma_f32_16x16x128_f8f6f4 v[64:67], v[0:7], v[218:225], v[64:67]
	v_mfma_f32_16x16x128_f8f6f4 v[56:59], v[8:15], v[226:233], v[56:59]
	v_mfma_f32_16x16x128_f8f6f4 v[48:51], v[0:7], v[226:233], v[48:51]
	v_mfma_f32_16x16x128_f8f6f4 v[40:43], v[8:15], v[234:241], v[40:43]
	v_mfma_f32_16x16x128_f8f6f4 v[32:35], v[0:7], v[234:241], v[32:35]
	s_setprio 0
	s_barrier
	ds_read_b128 v[0:3], v252 offset:32768
	ds_read_b128 v[4:7], v253 offset:32768
	ds_read_b128 v[8:11], v252 offset:34816
	ds_read_b128 v[12:15], v253 offset:34816
	ds_read_b128 v[16:19], v252 offset:49152
	ds_read_b128 v[20:23], v253 offset:49152
	ds_read_b128 v[24:27], v252 offset:51200
	ds_read_b128 v[28:31], v253 offset:51200
	s_mov_b32 m0, s63
	ds_read_b128 v[210:213], v201 offset:32768
	ds_read_b128 v[218:221], v201 offset:34816
	ds_read_b128 v[214:217], v202 offset:32768
	ds_read_b128 v[222:225], v202 offset:34816
	ds_read_b128 v[226:229], v201 offset:36864
	ds_read_b128 v[234:237], v201 offset:38912
	ds_read_b128 v[230:233], v202 offset:36864
	ds_read_b128 v[238:241], v202 offset:38912
	global_load_lds_dwordx4 v180, s[36:37]
	s_mov_b32 m0, s64
	s_nop 0
	global_load_lds_dwordx4 v178, s[36:37]
	s_waitcnt vmcnt(8)
	s_waitcnt lgkmcnt(0)
	s_barrier
	s_setprio 1
	s_waitcnt lgkmcnt(0)
	v_mfma_f32_16x16x128_f8f6f4 v[156:159], v[0:7], v[210:217], v[156:159]
	v_mfma_f32_16x16x128_f8f6f4 v[148:151], v[8:15], v[210:217], v[148:151]
	v_mfma_f32_16x16x128_f8f6f4 v[140:143], v[0:7], v[218:225], v[140:143]
	v_mfma_f32_16x16x128_f8f6f4 v[132:135], v[8:15], v[218:225], v[132:135]
	v_mfma_f32_16x16x128_f8f6f4 v[124:127], v[0:7], v[226:233], v[124:127]
	v_mfma_f32_16x16x128_f8f6f4 v[116:119], v[8:15], v[226:233], v[116:119]
	v_mfma_f32_16x16x128_f8f6f4 v[108:111], v[0:7], v[234:241], v[108:111]
	v_mfma_f32_16x16x128_f8f6f4 v[100:103], v[8:15], v[234:241], v[100:103]
	v_mfma_f32_16x16x128_f8f6f4 v[152:155], v[16:23], v[210:217], v[152:155]
	v_mfma_f32_16x16x128_f8f6f4 v[144:147], v[24:31], v[210:217], v[144:147]
	v_mfma_f32_16x16x128_f8f6f4 v[136:139], v[16:23], v[218:225], v[136:139]
	v_mfma_f32_16x16x128_f8f6f4 v[128:131], v[24:31], v[218:225], v[128:131]
	v_mfma_f32_16x16x128_f8f6f4 v[120:123], v[16:23], v[226:233], v[120:123]
	v_mfma_f32_16x16x128_f8f6f4 v[112:115], v[24:31], v[226:233], v[112:115]
	v_mfma_f32_16x16x128_f8f6f4 v[104:107], v[16:23], v[234:241], v[104:107]
	v_mfma_f32_16x16x128_f8f6f4 v[96:99], v[24:31], v[234:241], v[96:99]
	s_setprio 0
	s_barrier
	s_add_i32 s99, s44, 0x17f80
	s_mov_b32 m0, s99
	ds_read_b128 v[210:213], v201 offset:49152
	ds_read_b128 v[218:221], v201 offset:51200
	ds_read_b128 v[214:217], v202 offset:49152
	ds_read_b128 v[222:225], v202 offset:51200
	ds_read_b128 v[226:229], v201 offset:53248
	ds_read_b128 v[234:237], v201 offset:55296
	ds_read_b128 v[230:233], v202 offset:53248
	ds_read_b128 v[238:241], v202 offset:55296
	global_load_lds_dwordx4 v160, s[38:39] offset:128
	s_add_i32 m0, s99, 0x2000
	s_add_i32 s99, s44, 0x1bf80
	global_load_lds_dwordx4 v162, s[38:39] offset:128
	s_mov_b32 m0, s99
	s_nop 0
	global_load_lds_dwordx4 v160, s[40:41] offset:128
	s_add_i32 m0, s99, 0x2000
	s_nop 0
	global_load_lds_dwordx4 v162, s[40:41] offset:128
	s_waitcnt vmcnt(6)
	s_waitcnt lgkmcnt(0)
	s_barrier
	s_setprio 1
	s_waitcnt lgkmcnt(0)
	v_mfma_f32_16x16x128_f8f6f4 v[92:95], v[0:7], v[210:217], v[92:95]
	v_mfma_f32_16x16x128_f8f6f4 v[84:87], v[8:15], v[210:217], v[84:87]
	v_mfma_f32_16x16x128_f8f6f4 v[76:79], v[0:7], v[218:225], v[76:79]
	v_mfma_f32_16x16x128_f8f6f4 v[68:71], v[8:15], v[218:225], v[68:71]
	s_add_i32 m0, s65, 0xffffff80
	v_mfma_f32_16x16x128_f8f6f4 v[60:63], v[0:7], v[226:233], v[60:63]
	global_load_lds_dwordx4 v164, s[36:37] offset:128
	v_mfma_f32_16x16x128_f8f6f4 v[52:55], v[8:15], v[226:233], v[52:55]
	v_mfma_f32_16x16x128_f8f6f4 v[44:47], v[0:7], v[234:241], v[44:47]
	v_mfma_f32_16x16x128_f8f6f4 v[36:39], v[8:15], v[234:241], v[36:39]
	v_mfma_f32_16x16x128_f8f6f4 v[88:91], v[16:23], v[210:217], v[88:91]
	s_add_i32 m0, s66, 0xffffff80
	v_mfma_f32_16x16x128_f8f6f4 v[80:83], v[24:31], v[210:217], v[80:83]
	global_load_lds_dwordx4 v166, s[36:37] offset:128
	v_mfma_f32_16x16x128_f8f6f4 v[72:75], v[16:23], v[218:225], v[72:75]
	v_mfma_f32_16x16x128_f8f6f4 v[64:67], v[24:31], v[218:225], v[64:67]
	v_mfma_f32_16x16x128_f8f6f4 v[56:59], v[16:23], v[226:233], v[56:59]
	v_mfma_f32_16x16x128_f8f6f4 v[48:51], v[24:31], v[226:233], v[48:51]
	v_mfma_f32_16x16x128_f8f6f4 v[40:43], v[16:23], v[234:241], v[40:43]
	v_mfma_f32_16x16x128_f8f6f4 v[32:35], v[24:31], v[234:241], v[32:35]
	s_setprio 0
	s_barrier
	s_add_i32 s89, s89, 2
	s_add_u32 s4, s4, 0x100
	s_addc_u32 s5, s5, 0
	s_cmp_gt_u32 s89, 5
	s_cbranch_scc1 .LBB0_593

.LBB0_672:
	s_add_u32 s36, s6, s34
	s_addc_u32 s37, s7, s35
	s_add_u32 s38, s36, 0x12c00100
	s_addc_u32 s39, s37, 0
	ds_read_b128 v[24:27], v252
	ds_read_b128 v[28:31], v253
	s_and_b64 s[36:37], s[40:41], exec
	ds_read_b128 v[16:19], v252 offset:2048
	ds_read_b128 v[20:23], v253 offset:2048
	s_cselect_b32 s37, s9, s39
	s_cselect_b32 s36, s8, s38
	s_add_u32 s86, s27, s34
	ds_read_b128 v[8:11], v252 offset:16384
	ds_read_b128 v[12:15], v253 offset:16384
	s_addc_u32 s87, s82, s35
	ds_read_b128 v[0:3], v252 offset:18432
	ds_read_b128 v[4:7], v253 offset:18432
	s_and_b64 s[38:39], s[40:41], exec
	s_cselect_b32 s39, s29, s87
	s_cselect_b32 s38, s28, s86
	s_add_u32 s86, s83, s34
	s_addc_u32 s87, s84, s35
	s_and_b64 s[40:41], s[40:41], exec
	s_cselect_b32 s41, s31, s87
	s_cselect_b32 s40, s30, s86
	s_add_u32 s100, s16, s34
	s_addc_u32 s101, s17, s35
	s_add_i32 m0, s59, 0xc000
	ds_read_b128 v[186:189], v207
	ds_read_b128 v[216:219], v207 offset:2048
	ds_read_b128 v[190:193], v208
	ds_read_b128 v[220:223], v208 offset:2048
	ds_read_b128 v[224:227], v207 offset:4096
	ds_read_b128 v[232:235], v207 offset:6144
	ds_read_b128 v[228:231], v208 offset:4096
	ds_read_b128 v[236:239], v208 offset:6144
	global_load_lds_dwordx4 v166, s[100:101]
	s_add_i32 m0, s59, 0xe000
	s_nop 0
	global_load_lds_dwordx4 v168, s[100:101]
	s_waitcnt vmcnt(8)
	s_waitcnt lgkmcnt(0)
	s_barrier
	s_setprio 1
	s_waitcnt lgkmcnt(0)
	v_mfma_f32_16x16x128_f8f6f4 v[156:159], v[24:31], v[186:193], v[156:159]
	v_mfma_f32_16x16x128_f8f6f4 v[152:155], v[16:23], v[186:193], v[152:155]
	v_mfma_f32_16x16x128_f8f6f4 v[140:143], v[24:31], v[216:223], v[140:143]
	v_mfma_f32_16x16x128_f8f6f4 v[136:139], v[16:23], v[216:223], v[136:139]
	v_mfma_f32_16x16x128_f8f6f4 v[124:127], v[24:31], v[224:231], v[124:127]
	v_mfma_f32_16x16x128_f8f6f4 v[120:123], v[16:23], v[224:231], v[120:123]
	v_mfma_f32_16x16x128_f8f6f4 v[108:111], v[24:31], v[232:239], v[108:111]
	v_mfma_f32_16x16x128_f8f6f4 v[104:107], v[16:23], v[232:239], v[104:107]
	v_mfma_f32_16x16x128_f8f6f4 v[148:151], v[8:15], v[186:193], v[148:151]
	v_mfma_f32_16x16x128_f8f6f4 v[144:147], v[0:7], v[186:193], v[144:147]
	v_mfma_f32_16x16x128_f8f6f4 v[132:135], v[8:15], v[216:223], v[132:135]
	v_mfma_f32_16x16x128_f8f6f4 v[128:131], v[0:7], v[216:223], v[128:131]
	v_mfma_f32_16x16x128_f8f6f4 v[116:119], v[8:15], v[224:231], v[116:119]
	v_mfma_f32_16x16x128_f8f6f4 v[112:115], v[0:7], v[224:231], v[112:115]
	v_mfma_f32_16x16x128_f8f6f4 v[100:103], v[8:15], v[232:239], v[100:103]
	v_mfma_f32_16x16x128_f8f6f4 v[96:99], v[0:7], v[232:239], v[96:99]
	s_setprio 0
	s_barrier
	s_add_i32 s86, s69, s42
	s_mov_b32 m0, s86
	ds_read_b128 v[216:219], v207 offset:16384
	ds_read_b128 v[224:227], v207 offset:18432
	ds_read_b128 v[220:223], v208 offset:16384
	ds_read_b128 v[228:231], v208 offset:18432
	ds_read_b128 v[232:235], v207 offset:20480
	ds_read_b128 v[240:243], v207 offset:22528
	ds_read_b128 v[236:239], v208 offset:20480
	ds_read_b128 v[244:247], v208 offset:22528
	global_load_lds_dwordx4 v160, s[38:39]
	s_add_i32 m0, s86, 0x2000
	s_add_i32 s98, s71, s42
	global_load_lds_dwordx4 v162, s[38:39]
	s_mov_b32 m0, s98
	s_nop 0
	global_load_lds_dwordx4 v160, s[40:41]
	s_add_i32 m0, s98, 0x2000
	v_mov_b32_e32 v173, v165
	global_load_lds_dwordx4 v162, s[40:41]
	s_waitcnt vmcnt(6)
	s_waitcnt lgkmcnt(0)
	s_barrier
	s_setprio 1
	s_waitcnt lgkmcnt(0)
	v_mfma_f32_16x16x128_f8f6f4 v[92:95], v[24:31], v[216:223], v[92:95]
	v_mfma_f32_16x16x128_f8f6f4 v[88:91], v[16:23], v[216:223], v[88:91]
	v_mfma_f32_16x16x128_f8f6f4 v[76:79], v[24:31], v[224:231], v[76:79]
	v_mfma_f32_16x16x128_f8f6f4 v[72:75], v[16:23], v[224:231], v[72:75]
	s_mov_b32 m0, s59
	v_mfma_f32_16x16x128_f8f6f4 v[60:63], v[24:31], v[232:239], v[60:63]
	global_load_lds_dwordx4 v164, s[36:37]
	v_mfma_f32_16x16x128_f8f6f4 v[56:59], v[16:23], v[232:239], v[56:59]
	v_mfma_f32_16x16x128_f8f6f4 v[44:47], v[24:31], v[240:247], v[44:47]
	v_mfma_f32_16x16x128_f8f6f4 v[40:43], v[16:23], v[240:247], v[40:43]
	v_mfma_f32_16x16x128_f8f6f4 v[84:87], v[8:15], v[216:223], v[84:87]
	s_mov_b32 m0, s60
	v_mfma_f32_16x16x128_f8f6f4 v[80:83], v[0:7], v[216:223], v[80:83]
	global_load_lds_dwordx4 v172, s[36:37]
	v_mfma_f32_16x16x128_f8f6f4 v[68:71], v[8:15], v[224:231], v[68:71]
	v_mfma_f32_16x16x128_f8f6f4 v[64:67], v[0:7], v[224:231], v[64:67]
	v_mfma_f32_16x16x128_f8f6f4 v[52:55], v[8:15], v[232:239], v[52:55]
	v_mfma_f32_16x16x128_f8f6f4 v[48:51], v[0:7], v[232:239], v[48:51]
	v_mfma_f32_16x16x128_f8f6f4 v[36:39], v[8:15], v[240:247], v[36:39]
	v_mfma_f32_16x16x128_f8f6f4 v[32:35], v[0:7], v[240:247], v[32:35]
	s_setprio 0
	s_barrier
	ds_read_b128 v[0:3], v252 offset:32768
	ds_read_b128 v[4:7], v253 offset:32768
	ds_read_b128 v[8:11], v252 offset:34816
	ds_read_b128 v[12:15], v253 offset:34816
	ds_read_b128 v[16:19], v252 offset:49152
	ds_read_b128 v[20:23], v253 offset:49152
	ds_read_b128 v[24:27], v252 offset:51200
	ds_read_b128 v[28:31], v253 offset:51200
	s_mov_b32 m0, s61
	ds_read_b128 v[216:219], v207 offset:32768
	ds_read_b128 v[224:227], v207 offset:34816
	ds_read_b128 v[220:223], v208 offset:32768
	ds_read_b128 v[228:231], v208 offset:34816
	ds_read_b128 v[232:235], v207 offset:36864
	ds_read_b128 v[240:243], v207 offset:38912
	ds_read_b128 v[236:239], v208 offset:36864
	ds_read_b128 v[244:247], v208 offset:38912
	global_load_lds_dwordx4 v184, s[36:37]
	s_mov_b32 m0, s62
	s_nop 0
	global_load_lds_dwordx4 v182, s[36:37]
	s_waitcnt vmcnt(8)
	s_waitcnt lgkmcnt(0)
	s_barrier
	s_setprio 1
	s_waitcnt lgkmcnt(0)
	v_mfma_f32_16x16x128_f8f6f4 v[156:159], v[0:7], v[216:223], v[156:159]
	v_mfma_f32_16x16x128_f8f6f4 v[152:155], v[8:15], v[216:223], v[152:155]
	v_mfma_f32_16x16x128_f8f6f4 v[140:143], v[0:7], v[224:231], v[140:143]
	v_mfma_f32_16x16x128_f8f6f4 v[136:139], v[8:15], v[224:231], v[136:139]
	v_mfma_f32_16x16x128_f8f6f4 v[124:127], v[0:7], v[232:239], v[124:127]
	v_mfma_f32_16x16x128_f8f6f4 v[120:123], v[8:15], v[232:239], v[120:123]
	v_mfma_f32_16x16x128_f8f6f4 v[108:111], v[0:7], v[240:247], v[108:111]
	v_mfma_f32_16x16x128_f8f6f4 v[104:107], v[8:15], v[240:247], v[104:107]
	v_mfma_f32_16x16x128_f8f6f4 v[148:151], v[16:23], v[216:223], v[148:151]
	v_mfma_f32_16x16x128_f8f6f4 v[144:147], v[24:31], v[216:223], v[144:147]
	v_mfma_f32_16x16x128_f8f6f4 v[132:135], v[16:23], v[224:231], v[132:135]
	v_mfma_f32_16x16x128_f8f6f4 v[128:131], v[24:31], v[224:231], v[128:131]
	v_mfma_f32_16x16x128_f8f6f4 v[116:119], v[16:23], v[232:239], v[116:119]
	v_mfma_f32_16x16x128_f8f6f4 v[112:115], v[24:31], v[232:239], v[112:115]
	v_mfma_f32_16x16x128_f8f6f4 v[100:103], v[16:23], v[240:247], v[100:103]
	v_mfma_f32_16x16x128_f8f6f4 v[96:99], v[24:31], v[240:247], v[96:99]
	s_setprio 0
	s_barrier
	s_add_i32 s99, s42, 0x17f80
	s_mov_b32 m0, s99
	ds_read_b128 v[216:219], v207 offset:49152
	ds_read_b128 v[224:227], v207 offset:51200
	ds_read_b128 v[220:223], v208 offset:49152
	ds_read_b128 v[228:231], v208 offset:51200
	ds_read_b128 v[232:235], v207 offset:53248
	ds_read_b128 v[240:243], v207 offset:55296
	ds_read_b128 v[236:239], v208 offset:53248
	ds_read_b128 v[244:247], v208 offset:55296
	global_load_lds_dwordx4 v160, s[38:39] offset:128
	s_add_i32 m0, s99, 0x2000
	s_add_i32 s99, s42, 0x1bf80
	global_load_lds_dwordx4 v162, s[38:39] offset:128
	s_mov_b32 m0, s99
	s_nop 0
	global_load_lds_dwordx4 v160, s[40:41] offset:128
	s_add_i32 m0, s99, 0x2000
	s_nop 0
	global_load_lds_dwordx4 v162, s[40:41] offset:128
	s_waitcnt vmcnt(6)
	s_waitcnt lgkmcnt(0)
	s_barrier
	s_setprio 1
	s_waitcnt lgkmcnt(0)
	v_mfma_f32_16x16x128_f8f6f4 v[92:95], v[0:7], v[216:223], v[92:95]
	v_mfma_f32_16x16x128_f8f6f4 v[88:91], v[8:15], v[216:223], v[88:91]
	v_mfma_f32_16x16x128_f8f6f4 v[76:79], v[0:7], v[224:231], v[76:79]
	v_mfma_f32_16x16x128_f8f6f4 v[72:75], v[8:15], v[224:231], v[72:75]
	s_add_i32 m0, s63, 0xffffff80
	v_mfma_f32_16x16x128_f8f6f4 v[60:63], v[0:7], v[232:239], v[60:63]
	global_load_lds_dwordx4 v164, s[36:37] offset:128
	v_mfma_f32_16x16x128_f8f6f4 v[56:59], v[8:15], v[232:239], v[56:59]
	v_mfma_f32_16x16x128_f8f6f4 v[44:47], v[0:7], v[240:247], v[44:47]
	v_mfma_f32_16x16x128_f8f6f4 v[40:43], v[8:15], v[240:247], v[40:43]
	v_mfma_f32_16x16x128_f8f6f4 v[84:87], v[16:23], v[216:223], v[84:87]
	s_add_i32 m0, s64, 0xffffff80
	v_mfma_f32_16x16x128_f8f6f4 v[80:83], v[24:31], v[216:223], v[80:83]
	global_load_lds_dwordx4 v172, s[36:37] offset:128
	v_mfma_f32_16x16x128_f8f6f4 v[68:71], v[16:23], v[224:231], v[68:71]
	v_mfma_f32_16x16x128_f8f6f4 v[64:67], v[24:31], v[224:231], v[64:67]
	v_mfma_f32_16x16x128_f8f6f4 v[52:55], v[16:23], v[232:239], v[52:55]
	v_mfma_f32_16x16x128_f8f6f4 v[48:51], v[24:31], v[232:239], v[48:51]
	v_mfma_f32_16x16x128_f8f6f4 v[36:39], v[16:23], v[240:247], v[36:39]
	v_mfma_f32_16x16x128_f8f6f4 v[32:35], v[24:31], v[240:247], v[32:35]
	s_setprio 0
	s_barrier
	s_add_i32 s85, s85, 2
	s_add_u32 s34, s34, 0x100
	s_addc_u32 s35, s35, 0
	s_cmp_gt_u32 s85, 5
	s_cbranch_scc1 .LBB0_675

.LBB0_817:
	s_add_u32 s28, s10, s26
	s_addc_u32 s29, s11, s27
	s_add_u32 s30, s28, 0x38000100
	s_addc_u32 s31, s29, 0
	ds_read_b128 v[24:27], v252
	ds_read_b128 v[28:31], v253
	s_and_b64 s[28:29], s[34:35], exec
	ds_read_b128 v[16:19], v252 offset:2048
	ds_read_b128 v[20:23], v253 offset:2048
	s_cselect_b32 s29, s1, s31
	s_cselect_b32 s28, s0, s30
	s_add_u32 s61, s56, s26
	ds_read_b128 v[8:11], v252 offset:16384
	ds_read_b128 v[12:15], v253 offset:16384
	s_addc_u32 s62, s57, s27
	ds_read_b128 v[0:3], v252 offset:18432
	ds_read_b128 v[4:7], v253 offset:18432
	s_and_b64 s[30:31], s[34:35], exec
	s_cselect_b32 s31, s23, s62
	s_cselect_b32 s30, s22, s61
	s_add_u32 s61, s58, s26
	s_addc_u32 s62, s59, s27
	s_and_b64 s[34:35], s[34:35], exec
	s_cselect_b32 s35, s25, s62
	s_cselect_b32 s34, s24, s61
	s_add_u32 s100, s14, s26
	s_addc_u32 s101, s15, s27
	s_add_i32 m0, s37, 0xc000
	ds_read_b128 v[186:189], v207
	ds_read_b128 v[216:219], v207 offset:2048
	ds_read_b128 v[190:193], v208
	ds_read_b128 v[220:223], v208 offset:2048
	ds_read_b128 v[224:227], v207 offset:4096
	ds_read_b128 v[232:235], v207 offset:6144
	ds_read_b128 v[228:231], v208 offset:4096
	ds_read_b128 v[236:239], v208 offset:6144
	global_load_lds_dwordx4 v168, s[100:101]
	s_add_i32 m0, s37, 0xe000
	s_nop 0
	global_load_lds_dwordx4 v170, s[100:101]
	s_waitcnt vmcnt(8)
	s_waitcnt lgkmcnt(0)
	s_barrier
	s_setprio 1
	s_waitcnt lgkmcnt(0)
	v_mfma_f32_16x16x128_f8f6f4 v[156:159], v[24:31], v[186:193], v[156:159]
	v_mfma_f32_16x16x128_f8f6f4 v[152:155], v[16:23], v[186:193], v[152:155]
	v_mfma_f32_16x16x128_f8f6f4 v[140:143], v[24:31], v[216:223], v[140:143]
	v_mfma_f32_16x16x128_f8f6f4 v[136:139], v[16:23], v[216:223], v[136:139]
	v_mfma_f32_16x16x128_f8f6f4 v[124:127], v[24:31], v[224:231], v[124:127]
	v_mfma_f32_16x16x128_f8f6f4 v[120:123], v[16:23], v[224:231], v[120:123]
	v_mfma_f32_16x16x128_f8f6f4 v[108:111], v[24:31], v[232:239], v[108:111]
	v_mfma_f32_16x16x128_f8f6f4 v[104:107], v[16:23], v[232:239], v[104:107]
	v_mfma_f32_16x16x128_f8f6f4 v[148:151], v[8:15], v[186:193], v[148:151]
	v_mfma_f32_16x16x128_f8f6f4 v[144:147], v[0:7], v[186:193], v[144:147]
	v_mfma_f32_16x16x128_f8f6f4 v[132:135], v[8:15], v[216:223], v[132:135]
	v_mfma_f32_16x16x128_f8f6f4 v[128:131], v[0:7], v[216:223], v[128:131]
	v_mfma_f32_16x16x128_f8f6f4 v[116:119], v[8:15], v[224:231], v[116:119]
	v_mfma_f32_16x16x128_f8f6f4 v[112:115], v[0:7], v[224:231], v[112:115]
	v_mfma_f32_16x16x128_f8f6f4 v[100:103], v[8:15], v[232:239], v[100:103]
	v_mfma_f32_16x16x128_f8f6f4 v[96:99], v[0:7], v[232:239], v[96:99]
	s_setprio 0
	s_barrier
	s_add_i32 s61, s44, s36
	s_mov_b32 m0, s61
	ds_read_b128 v[216:219], v207 offset:16384
	ds_read_b128 v[224:227], v207 offset:18432
	ds_read_b128 v[220:223], v208 offset:16384
	ds_read_b128 v[228:231], v208 offset:18432
	ds_read_b128 v[232:235], v207 offset:20480
	ds_read_b128 v[240:243], v207 offset:22528
	ds_read_b128 v[236:239], v208 offset:20480
	ds_read_b128 v[244:247], v208 offset:22528
	global_load_lds_dwordx4 v160, s[30:31]
	s_add_i32 m0, s61, 0x2000
	s_add_i32 s98, s46, s36
	global_load_lds_dwordx4 v162, s[30:31]
	s_mov_b32 m0, s98
	s_nop 0
	global_load_lds_dwordx4 v160, s[34:35]
	s_add_i32 m0, s98, 0x2000
	v_mov_b32_e32 v167, v165
	global_load_lds_dwordx4 v162, s[34:35]
	s_waitcnt vmcnt(6)
	s_waitcnt lgkmcnt(0)
	s_barrier
	s_setprio 1
	s_waitcnt lgkmcnt(0)
	v_mfma_f32_16x16x128_f8f6f4 v[92:95], v[24:31], v[216:223], v[92:95]
	v_mfma_f32_16x16x128_f8f6f4 v[88:91], v[16:23], v[216:223], v[88:91]
	v_mfma_f32_16x16x128_f8f6f4 v[76:79], v[24:31], v[224:231], v[76:79]
	v_mfma_f32_16x16x128_f8f6f4 v[72:75], v[16:23], v[224:231], v[72:75]
	s_mov_b32 m0, s37
	v_mfma_f32_16x16x128_f8f6f4 v[60:63], v[24:31], v[232:239], v[60:63]
	global_load_lds_dwordx4 v164, s[28:29]
	v_mfma_f32_16x16x128_f8f6f4 v[56:59], v[16:23], v[232:239], v[56:59]
	v_mfma_f32_16x16x128_f8f6f4 v[44:47], v[24:31], v[240:247], v[44:47]
	v_mfma_f32_16x16x128_f8f6f4 v[40:43], v[16:23], v[240:247], v[40:43]
	v_mfma_f32_16x16x128_f8f6f4 v[84:87], v[8:15], v[216:223], v[84:87]
	s_mov_b32 m0, s38
	v_mfma_f32_16x16x128_f8f6f4 v[80:83], v[0:7], v[216:223], v[80:83]
	global_load_lds_dwordx4 v166, s[28:29]
	v_mfma_f32_16x16x128_f8f6f4 v[68:71], v[8:15], v[224:231], v[68:71]
	v_mfma_f32_16x16x128_f8f6f4 v[64:67], v[0:7], v[224:231], v[64:67]
	v_mfma_f32_16x16x128_f8f6f4 v[52:55], v[8:15], v[232:239], v[52:55]
	v_mfma_f32_16x16x128_f8f6f4 v[48:51], v[0:7], v[232:239], v[48:51]
	v_mfma_f32_16x16x128_f8f6f4 v[36:39], v[8:15], v[240:247], v[36:39]
	v_mfma_f32_16x16x128_f8f6f4 v[32:35], v[0:7], v[240:247], v[32:35]
	s_setprio 0
	s_barrier
	ds_read_b128 v[0:3], v252 offset:32768
	ds_read_b128 v[4:7], v253 offset:32768
	ds_read_b128 v[8:11], v252 offset:34816
	ds_read_b128 v[12:15], v253 offset:34816
	ds_read_b128 v[16:19], v252 offset:49152
	ds_read_b128 v[20:23], v253 offset:49152
	ds_read_b128 v[24:27], v252 offset:51200
	ds_read_b128 v[28:31], v253 offset:51200
	s_mov_b32 m0, s39
	ds_read_b128 v[216:219], v207 offset:32768
	ds_read_b128 v[224:227], v207 offset:34816
	ds_read_b128 v[220:223], v208 offset:32768
	ds_read_b128 v[228:231], v208 offset:34816
	ds_read_b128 v[232:235], v207 offset:36864
	ds_read_b128 v[240:243], v207 offset:38912
	ds_read_b128 v[236:239], v208 offset:36864
	ds_read_b128 v[244:247], v208 offset:38912
	global_load_lds_dwordx4 v184, s[28:29]
	s_mov_b32 m0, s40
	s_nop 0
	global_load_lds_dwordx4 v182, s[28:29]
	s_waitcnt vmcnt(8)
	s_waitcnt lgkmcnt(0)
	s_barrier
	s_setprio 1
	s_waitcnt lgkmcnt(0)
	v_mfma_f32_16x16x128_f8f6f4 v[156:159], v[0:7], v[216:223], v[156:159]
	v_mfma_f32_16x16x128_f8f6f4 v[152:155], v[8:15], v[216:223], v[152:155]
	v_mfma_f32_16x16x128_f8f6f4 v[140:143], v[0:7], v[224:231], v[140:143]
	v_mfma_f32_16x16x128_f8f6f4 v[136:139], v[8:15], v[224:231], v[136:139]
	v_mfma_f32_16x16x128_f8f6f4 v[124:127], v[0:7], v[232:239], v[124:127]
	v_mfma_f32_16x16x128_f8f6f4 v[120:123], v[8:15], v[232:239], v[120:123]
	v_mfma_f32_16x16x128_f8f6f4 v[108:111], v[0:7], v[240:247], v[108:111]
	v_mfma_f32_16x16x128_f8f6f4 v[104:107], v[8:15], v[240:247], v[104:107]
	v_mfma_f32_16x16x128_f8f6f4 v[148:151], v[16:23], v[216:223], v[148:151]
	v_mfma_f32_16x16x128_f8f6f4 v[144:147], v[24:31], v[216:223], v[144:147]
	v_mfma_f32_16x16x128_f8f6f4 v[132:135], v[16:23], v[224:231], v[132:135]
	v_mfma_f32_16x16x128_f8f6f4 v[128:131], v[24:31], v[224:231], v[128:131]
	v_mfma_f32_16x16x128_f8f6f4 v[116:119], v[16:23], v[232:239], v[116:119]
	v_mfma_f32_16x16x128_f8f6f4 v[112:115], v[24:31], v[232:239], v[112:115]
	v_mfma_f32_16x16x128_f8f6f4 v[100:103], v[16:23], v[240:247], v[100:103]
	v_mfma_f32_16x16x128_f8f6f4 v[96:99], v[24:31], v[240:247], v[96:99]
	s_setprio 0
	s_barrier
	s_add_i32 s99, s36, 0x17f80
	s_mov_b32 m0, s99
	ds_read_b128 v[216:219], v207 offset:49152
	ds_read_b128 v[224:227], v207 offset:51200
	ds_read_b128 v[220:223], v208 offset:49152
	ds_read_b128 v[228:231], v208 offset:51200
	ds_read_b128 v[232:235], v207 offset:53248
	ds_read_b128 v[240:243], v207 offset:55296
	ds_read_b128 v[236:239], v208 offset:53248
	ds_read_b128 v[244:247], v208 offset:55296
	global_load_lds_dwordx4 v160, s[30:31] offset:128
	s_add_i32 m0, s99, 0x2000
	s_add_i32 s99, s36, 0x1bf80
	global_load_lds_dwordx4 v162, s[30:31] offset:128
	s_mov_b32 m0, s99
	s_nop 0
	global_load_lds_dwordx4 v160, s[34:35] offset:128
	s_add_i32 m0, s99, 0x2000
	s_nop 0
	global_load_lds_dwordx4 v162, s[34:35] offset:128
	s_waitcnt vmcnt(6)
	s_waitcnt lgkmcnt(0)
	s_barrier
	s_setprio 1
	s_waitcnt lgkmcnt(0)
	v_mfma_f32_16x16x128_f8f6f4 v[92:95], v[0:7], v[216:223], v[92:95]
	v_mfma_f32_16x16x128_f8f6f4 v[88:91], v[8:15], v[216:223], v[88:91]
	v_mfma_f32_16x16x128_f8f6f4 v[76:79], v[0:7], v[224:231], v[76:79]
	v_mfma_f32_16x16x128_f8f6f4 v[72:75], v[8:15], v[224:231], v[72:75]
	s_add_i32 m0, s41, 0xffffff80
	v_mfma_f32_16x16x128_f8f6f4 v[60:63], v[0:7], v[232:239], v[60:63]
	global_load_lds_dwordx4 v164, s[28:29] offset:128
	v_mfma_f32_16x16x128_f8f6f4 v[56:59], v[8:15], v[232:239], v[56:59]
	v_mfma_f32_16x16x128_f8f6f4 v[44:47], v[0:7], v[240:247], v[44:47]
	v_mfma_f32_16x16x128_f8f6f4 v[40:43], v[8:15], v[240:247], v[40:43]
	v_mfma_f32_16x16x128_f8f6f4 v[84:87], v[16:23], v[216:223], v[84:87]
	s_add_i32 m0, s42, 0xffffff80
	v_mfma_f32_16x16x128_f8f6f4 v[80:83], v[24:31], v[216:223], v[80:83]
	global_load_lds_dwordx4 v166, s[28:29] offset:128
	v_mfma_f32_16x16x128_f8f6f4 v[68:71], v[16:23], v[224:231], v[68:71]
	v_mfma_f32_16x16x128_f8f6f4 v[64:67], v[24:31], v[224:231], v[64:67]
	v_mfma_f32_16x16x128_f8f6f4 v[52:55], v[16:23], v[232:239], v[52:55]
	v_mfma_f32_16x16x128_f8f6f4 v[48:51], v[24:31], v[232:239], v[48:51]
	v_mfma_f32_16x16x128_f8f6f4 v[36:39], v[16:23], v[240:247], v[36:39]
	v_mfma_f32_16x16x128_f8f6f4 v[32:35], v[24:31], v[240:247], v[32:35]
	s_setprio 0
	s_barrier
	s_add_i32 s60, s60, 2
	s_add_u32 s26, s26, 0x100
	s_addc_u32 s27, s27, 0
	s_cmp_gt_u32 s60, 5
	s_cbranch_scc1 .LBB0_820

.LBB0_1549:
	s_add_u32 s26, s4, s24
	s_addc_u32 s27, s5, s25
	s_add_u32 s28, s26, 0x28000100
	s_addc_u32 s29, s27, 0
	ds_read_b128 v[24:27], v252
	ds_read_b128 v[28:31], v253
	s_and_b64 s[26:27], s[30:31], exec
	ds_read_b128 v[16:19], v252 offset:2048
	ds_read_b128 v[20:23], v253 offset:2048
	s_cselect_b32 s27, s7, s29
	s_cselect_b32 s26, s6, s28
	s_add_u32 s63, s58, s24
	ds_read_b128 v[8:11], v252 offset:16384
	ds_read_b128 v[12:15], v253 offset:16384
	s_addc_u32 s64, s59, s25
	ds_read_b128 v[0:3], v252 offset:18432
	ds_read_b128 v[4:7], v253 offset:18432
	s_and_b64 s[28:29], s[30:31], exec
	s_cselect_b32 s29, s21, s64
	s_cselect_b32 s28, s20, s63
	s_add_u32 s63, s60, s24
	s_addc_u32 s64, s61, s25
	s_and_b64 s[30:31], s[30:31], exec
	s_cselect_b32 s31, s23, s64
	s_cselect_b32 s30, s22, s63
	s_add_u32 s100, s14, s24
	s_addc_u32 s101, s15, s25
	s_add_i32 m0, s35, 0xc000
	ds_read_b128 v[186:189], v206
	ds_read_b128 v[214:217], v206 offset:2048
	ds_read_b128 v[190:193], v207
	ds_read_b128 v[218:221], v207 offset:2048
	ds_read_b128 v[222:225], v206 offset:4096
	ds_read_b128 v[230:233], v206 offset:6144
	ds_read_b128 v[226:229], v207 offset:4096
	ds_read_b128 v[234:237], v207 offset:6144
	global_load_lds_dwordx4 v168, s[100:101]
	s_add_i32 m0, s35, 0xe000
	s_nop 0
	global_load_lds_dwordx4 v170, s[100:101]
	s_waitcnt vmcnt(8)
	s_waitcnt lgkmcnt(0)
	s_barrier
	s_setprio 1
	s_waitcnt lgkmcnt(0)
	v_mfma_f32_16x16x128_f8f6f4 v[156:159], v[24:31], v[186:193], v[156:159]
	v_mfma_f32_16x16x128_f8f6f4 v[152:155], v[16:23], v[186:193], v[152:155]
	v_mfma_f32_16x16x128_f8f6f4 v[144:147], v[24:31], v[214:221], v[144:147]
	v_mfma_f32_16x16x128_f8f6f4 v[136:139], v[16:23], v[214:221], v[136:139]
	v_mfma_f32_16x16x128_f8f6f4 v[124:127], v[24:31], v[222:229], v[124:127]
	v_mfma_f32_16x16x128_f8f6f4 v[120:123], v[16:23], v[222:229], v[120:123]
	v_mfma_f32_16x16x128_f8f6f4 v[112:115], v[24:31], v[230:237], v[112:115]
	v_mfma_f32_16x16x128_f8f6f4 v[104:107], v[16:23], v[230:237], v[104:107]
	v_mfma_f32_16x16x128_f8f6f4 v[148:151], v[8:15], v[186:193], v[148:151]
	v_mfma_f32_16x16x128_f8f6f4 v[140:143], v[0:7], v[186:193], v[140:143]
	v_mfma_f32_16x16x128_f8f6f4 v[132:135], v[8:15], v[214:221], v[132:135]
	v_mfma_f32_16x16x128_f8f6f4 v[128:131], v[0:7], v[214:221], v[128:131]
	v_mfma_f32_16x16x128_f8f6f4 v[116:119], v[8:15], v[222:229], v[116:119]
	v_mfma_f32_16x16x128_f8f6f4 v[108:111], v[0:7], v[222:229], v[108:111]
	v_mfma_f32_16x16x128_f8f6f4 v[100:103], v[8:15], v[230:237], v[100:103]
	v_mfma_f32_16x16x128_f8f6f4 v[96:99], v[0:7], v[230:237], v[96:99]
	s_setprio 0
	s_barrier
	s_add_i32 s63, s46, s34
	s_mov_b32 m0, s63
	ds_read_b128 v[214:217], v206 offset:16384
	ds_read_b128 v[222:225], v206 offset:18432
	ds_read_b128 v[218:221], v207 offset:16384
	ds_read_b128 v[226:229], v207 offset:18432
	ds_read_b128 v[230:233], v206 offset:20480
	ds_read_b128 v[238:241], v206 offset:22528
	ds_read_b128 v[234:237], v207 offset:20480
	ds_read_b128 v[242:245], v207 offset:22528
	global_load_lds_dwordx4 v160, s[28:29]
	s_add_i32 m0, s63, 0x2000
	s_add_i32 s98, s48, s34
	global_load_lds_dwordx4 v162, s[28:29]
	s_mov_b32 m0, s98
	s_nop 0
	global_load_lds_dwordx4 v160, s[30:31]
	s_add_i32 m0, s98, 0x2000
	v_mov_b32_e32 v167, v165
	global_load_lds_dwordx4 v162, s[30:31]
	s_waitcnt vmcnt(6)
	s_waitcnt lgkmcnt(0)
	s_barrier
	s_setprio 1
	s_waitcnt lgkmcnt(0)
	v_mfma_f32_16x16x128_f8f6f4 v[92:95], v[24:31], v[214:221], v[92:95]
	v_mfma_f32_16x16x128_f8f6f4 v[88:91], v[16:23], v[214:221], v[88:91]
	v_mfma_f32_16x16x128_f8f6f4 v[80:83], v[24:31], v[222:229], v[80:83]
	v_mfma_f32_16x16x128_f8f6f4 v[72:75], v[16:23], v[222:229], v[72:75]
	s_mov_b32 m0, s35
	v_mfma_f32_16x16x128_f8f6f4 v[60:63], v[24:31], v[230:237], v[60:63]
	global_load_lds_dwordx4 v164, s[26:27]
	v_mfma_f32_16x16x128_f8f6f4 v[56:59], v[16:23], v[230:237], v[56:59]
	v_mfma_f32_16x16x128_f8f6f4 v[48:51], v[24:31], v[238:245], v[48:51]
	v_mfma_f32_16x16x128_f8f6f4 v[40:43], v[16:23], v[238:245], v[40:43]
	v_mfma_f32_16x16x128_f8f6f4 v[84:87], v[8:15], v[214:221], v[84:87]
	s_mov_b32 m0, s36
	v_mfma_f32_16x16x128_f8f6f4 v[76:79], v[0:7], v[214:221], v[76:79]
	global_load_lds_dwordx4 v166, s[26:27]
	v_mfma_f32_16x16x128_f8f6f4 v[68:71], v[8:15], v[222:229], v[68:71]
	v_mfma_f32_16x16x128_f8f6f4 v[64:67], v[0:7], v[222:229], v[64:67]
	v_mfma_f32_16x16x128_f8f6f4 v[52:55], v[8:15], v[230:237], v[52:55]
	v_mfma_f32_16x16x128_f8f6f4 v[44:47], v[0:7], v[230:237], v[44:47]
	v_mfma_f32_16x16x128_f8f6f4 v[36:39], v[8:15], v[238:245], v[36:39]
	v_mfma_f32_16x16x128_f8f6f4 v[32:35], v[0:7], v[238:245], v[32:35]
	s_setprio 0
	s_barrier
	ds_read_b128 v[0:3], v252 offset:32768
	ds_read_b128 v[4:7], v253 offset:32768
	ds_read_b128 v[8:11], v252 offset:34816
	ds_read_b128 v[12:15], v253 offset:34816
	ds_read_b128 v[16:19], v252 offset:49152
	ds_read_b128 v[20:23], v253 offset:49152
	ds_read_b128 v[24:27], v252 offset:51200
	ds_read_b128 v[28:31], v253 offset:51200
	s_mov_b32 m0, s37
	ds_read_b128 v[214:217], v206 offset:32768
	ds_read_b128 v[222:225], v206 offset:34816
	ds_read_b128 v[218:221], v207 offset:32768
	ds_read_b128 v[226:229], v207 offset:34816
	ds_read_b128 v[230:233], v206 offset:36864
	ds_read_b128 v[238:241], v206 offset:38912
	ds_read_b128 v[234:237], v207 offset:36864
	ds_read_b128 v[242:245], v207 offset:38912
	global_load_lds_dwordx4 v184, s[26:27]
	s_mov_b32 m0, s38
	s_nop 0
	global_load_lds_dwordx4 v182, s[26:27]
	s_waitcnt vmcnt(8)
	s_waitcnt lgkmcnt(0)
	s_barrier
	s_setprio 1
	s_waitcnt lgkmcnt(0)
	v_mfma_f32_16x16x128_f8f6f4 v[156:159], v[0:7], v[214:221], v[156:159]
	v_mfma_f32_16x16x128_f8f6f4 v[152:155], v[8:15], v[214:221], v[152:155]
	v_mfma_f32_16x16x128_f8f6f4 v[144:147], v[0:7], v[222:229], v[144:147]
	v_mfma_f32_16x16x128_f8f6f4 v[136:139], v[8:15], v[222:229], v[136:139]
	v_mfma_f32_16x16x128_f8f6f4 v[124:127], v[0:7], v[230:237], v[124:127]
	v_mfma_f32_16x16x128_f8f6f4 v[120:123], v[8:15], v[230:237], v[120:123]
	v_mfma_f32_16x16x128_f8f6f4 v[112:115], v[0:7], v[238:245], v[112:115]
	v_mfma_f32_16x16x128_f8f6f4 v[104:107], v[8:15], v[238:245], v[104:107]
	v_mfma_f32_16x16x128_f8f6f4 v[148:151], v[16:23], v[214:221], v[148:151]
	v_mfma_f32_16x16x128_f8f6f4 v[140:143], v[24:31], v[214:221], v[140:143]
	v_mfma_f32_16x16x128_f8f6f4 v[132:135], v[16:23], v[222:229], v[132:135]
	v_mfma_f32_16x16x128_f8f6f4 v[128:131], v[24:31], v[222:229], v[128:131]
	v_mfma_f32_16x16x128_f8f6f4 v[116:119], v[16:23], v[230:237], v[116:119]
	v_mfma_f32_16x16x128_f8f6f4 v[108:111], v[24:31], v[230:237], v[108:111]
	v_mfma_f32_16x16x128_f8f6f4 v[100:103], v[16:23], v[238:245], v[100:103]
	v_mfma_f32_16x16x128_f8f6f4 v[96:99], v[24:31], v[238:245], v[96:99]
	s_setprio 0
	s_barrier
	s_add_i32 s99, s34, 0x17f80
	s_mov_b32 m0, s99
	ds_read_b128 v[214:217], v206 offset:49152
	ds_read_b128 v[222:225], v206 offset:51200
	ds_read_b128 v[218:221], v207 offset:49152
	ds_read_b128 v[226:229], v207 offset:51200
	ds_read_b128 v[230:233], v206 offset:53248
	ds_read_b128 v[238:241], v206 offset:55296
	ds_read_b128 v[234:237], v207 offset:53248
	ds_read_b128 v[242:245], v207 offset:55296
	global_load_lds_dwordx4 v160, s[28:29] offset:128
	s_add_i32 m0, s99, 0x2000
	s_add_i32 s99, s34, 0x1bf80
	global_load_lds_dwordx4 v162, s[28:29] offset:128
	s_mov_b32 m0, s99
	s_nop 0
	global_load_lds_dwordx4 v160, s[30:31] offset:128
	s_add_i32 m0, s99, 0x2000
	s_nop 0
	global_load_lds_dwordx4 v162, s[30:31] offset:128
	s_waitcnt vmcnt(6)
	s_waitcnt lgkmcnt(0)
	s_barrier
	s_setprio 1
	s_waitcnt lgkmcnt(0)
	v_mfma_f32_16x16x128_f8f6f4 v[92:95], v[0:7], v[214:221], v[92:95]
	v_mfma_f32_16x16x128_f8f6f4 v[88:91], v[8:15], v[214:221], v[88:91]
	v_mfma_f32_16x16x128_f8f6f4 v[80:83], v[0:7], v[222:229], v[80:83]
	v_mfma_f32_16x16x128_f8f6f4 v[72:75], v[8:15], v[222:229], v[72:75]
	s_add_i32 m0, s41, 0xffffff80
	v_mfma_f32_16x16x128_f8f6f4 v[60:63], v[0:7], v[230:237], v[60:63]
	global_load_lds_dwordx4 v164, s[26:27] offset:128
	v_mfma_f32_16x16x128_f8f6f4 v[56:59], v[8:15], v[230:237], v[56:59]
	v_mfma_f32_16x16x128_f8f6f4 v[48:51], v[0:7], v[238:245], v[48:51]
	v_mfma_f32_16x16x128_f8f6f4 v[40:43], v[8:15], v[238:245], v[40:43]
	v_mfma_f32_16x16x128_f8f6f4 v[84:87], v[16:23], v[214:221], v[84:87]
	s_add_i32 m0, s42, 0xffffff80
	v_mfma_f32_16x16x128_f8f6f4 v[76:79], v[24:31], v[214:221], v[76:79]
	global_load_lds_dwordx4 v166, s[26:27] offset:128
	v_mfma_f32_16x16x128_f8f6f4 v[68:71], v[16:23], v[222:229], v[68:71]
	v_mfma_f32_16x16x128_f8f6f4 v[64:67], v[24:31], v[222:229], v[64:67]
	v_mfma_f32_16x16x128_f8f6f4 v[52:55], v[16:23], v[230:237], v[52:55]
	v_mfma_f32_16x16x128_f8f6f4 v[44:47], v[24:31], v[230:237], v[44:47]
	v_mfma_f32_16x16x128_f8f6f4 v[36:39], v[16:23], v[238:245], v[36:39]
	v_mfma_f32_16x16x128_f8f6f4 v[32:35], v[24:31], v[238:245], v[32:35]
	s_setprio 0
	s_barrier
	s_add_i32 s62, s62, 2
	s_add_u32 s24, s24, 0x100
	s_addc_u32 s25, s25, 0
	s_cmp_gt_u32 s62, 29
	s_cbranch_scc1 .LBB0_1552
